# baseline (speedup 1.0000x reference)
.Lpro_wc_done:
	s_lshr_b32 s0, s33, 8
	s_lshl_b32 s1, s37, 4
	v_and_or_b32 v104, s1, 48, v82
	s_waitcnt lgkmcnt(0)
	v_mov_b32_e32 v62, 0x15300
	v_lshl_or_b32 v62, v104, 2, v62
	v_lshlrev_b32_e32 v109, 5, v106
	s_barrier
	ds_read_b32 v105, v62
	v_or_b32_e32 v62, 0x15000, v109
	v_or_b32_e32 v84, 0x15100, v109
	ds_read_b128 v[62:65], v62
	ds_read_b128 v[84:87], v84
	s_lshl_b32 s1, s0, 6
	s_add_i32 s2, s1, 0x14c00
	v_lshlrev_b32_e32 v108, 4, v106
	v_or_b32_e32 v88, s2, v108
	s_waitcnt lgkmcnt(0)
	v_fma_f32 v63, v105, v63, v85
	v_lshlrev_b32_e32 v92, 4, v1
	v_max_f32_e32 v101, 0, v63
	v_or_b32_e32 v63, 0x15010, v109
	ds_read_b128 v[88:91], v88 offset:1536
	v_lshl_or_b32 v100, s0, 11, v92
	v_fma_f32 v62, v105, v62, v84
	v_or_b32_e32 v84, 0x15110, v109
	ds_read_b128 v[92:95], v63
	ds_read_b128 v[96:99], v84
	v_fmac_f32_e32 v87, v105, v65
	v_fma_f32 v63, v105, v64, v86
	v_max_f32_e32 v102, 0, v87
	v_max_f32_e32 v62, 0, v62
	s_waitcnt lgkmcnt(0)
	v_fma_f32 v65, v105, v93, v97
	v_fma_f32 v64, v105, v92, v96
	v_max_f32_e32 v92, 0, v65
	v_fma_f32 v65, v105, v94, v98
	v_fmac_f32_e32 v99, v105, v95
	v_max_f32_e32 v65, 0, v65
	v_max_f32_e32 v84, 0, v99
	v_cvt_pk_f16_f32 v65, v65, v84
	ds_read_b128 v[84:87], v100 offset:36864
	v_max_f32_e32 v64, 0, v64
	v_cvt_pk_f16_f32 v64, v64, v92
	v_or_b32_e32 v92, 0x15080, v109
	v_or_b32_e32 v96, 0x15180, v109
	ds_read_b128 v[92:95], v92
	ds_read_b128 v[96:99], v96
	v_max_f32_e32 v63, 0, v63
	v_cvt_pk_f16_f32 v63, v63, v102
	v_cvt_pk_f16_f32 v62, v62, v101
	ds_read_b128 v[100:103], v100 offset:37888
	s_waitcnt lgkmcnt(1)
	v_fma_f32 v94, v105, v94, v98
	v_mfma_f32_16x16x32_f16 v[62:65], v[84:87], v[62:65], v[88:91]
	v_fma_f32 v84, v105, v92, v96
	v_max_f32_e32 v92, 0, v84
	v_fma_f32 v84, v105, v93, v97
	v_max_f32_e32 v93, 0, v84
	v_or_b32_e32 v84, 0x15090, v109
	v_or_b32_e32 v88, 0x15190, v109
	ds_read_b128 v[84:87], v84
	ds_read_b128 v[88:91], v88
	v_fmac_f32_e32 v99, v105, v95
	v_max_f32_e32 v94, 0, v94
	v_max_f32_e32 v95, 0, v99
	s_add_i32 s1, s1, 0xb000
	s_waitcnt lgkmcnt(0)
	v_fma_f32 v84, v105, v84, v88
	v_fma_f32 v85, v105, v85, v89
	v_fma_f32 v86, v105, v86, v90
	v_fmac_f32_e32 v91, v105, v87
	v_max_f32_e32 v84, 0, v84
	v_max_f32_e32 v85, 0, v85
	v_max_f32_e32 v86, 0, v86
	v_max_f32_e32 v87, 0, v91
	v_cvt_pk_f16_f32 v87, v86, v87
	v_cvt_pk_f16_f32 v86, v84, v85
	v_cvt_pk_f16_f32 v85, v94, v95
	v_cvt_pk_f16_f32 v84, v92, v93
	v_cmp_eq_u32_e64 s[12:13], 1, v106
	v_cmp_eq_u32_e64 s[2:3], 0, v1
	v_mfma_f32_16x16x32_f16 v[62:65], v[100:103], v[84:87], v[62:65]
	v_mul_u32_u24_e32 v84, 0x110, v104
	v_add3_u32 v84, s1, v84, v108
	v_or_b32_e32 v112, 4, v106
	v_or_b32_e32 v116, 60, v106
	s_nop 3
	ds_write_b128 v84, v[62:65]
	v_mbcnt_lo_u32_b32 v62, -1, 0
	v_mbcnt_hi_u32_b32 v62, -1, v62
	v_and_or_b32 v62, v62, 64, v82
	v_lshlrev_b32_e32 v108, 2, v62
	v_mov_b32_e32 v62, 0x13c00
	v_lshl_or_b32 v111, v106, 2, v62
	v_mov_b32_e32 v62, 0xf400
	v_lshl_or_b32 v113, v83, 2, v62
	v_and_b32_e32 v62, 8, v0
	v_cmp_eq_u32_e64 s[4:5], 0, v62
	v_and_b32_e32 v62, 4, v0
	v_cmp_eq_u32_e64 s[6:7], 0, v62
	v_and_b32_e32 v62, 2, v0
	v_and_b32_e32 v0, 1, v0
	v_cmp_eq_u32_e64 s[10:11], 0, v0
	v_mov_b32_e32 v0, 0x13400
	v_cmp_eq_u32_e64 s[8:9], 0, v62
	v_lshl_or_b32 v117, v1, 1, v0
	v_mov_b32_e32 v0, s14
	v_mov_b32_e32 v62, s26
	v_cndmask_b32_e64 v0, v0, v62, s[12:13]
	v_mov_b32_e32 v62, s15
	v_mov_b32_e32 v63, s27
	v_cndmask_b32_e64 v62, v62, v63, s[12:13]
	v_mov_b32_e32 v63, s25
	v_cmp_gt_u32_e64 s[14:15], 16, v1
	v_or_b32_e32 v109, 64, v108
	v_or_b32_e32 v110, 0x80, v108
	v_cndmask_b32_e64 v1, v62, v63, s[14:15]
	v_mov_b32_e32 v62, s24
	v_cndmask_b32_e64 v0, v0, v62, s[14:15]
	v_mov_b32_e32 v62, 0
	s_waitcnt lgkmcnt(0)
	s_barrier
	s_cmp_lt_u32 s37, 8
	s_cbranch_scc0 .Lh1_done
	v_mbcnt_lo_u32_b32 v82, -1, 0
	v_mbcnt_hi_u32_b32 v82, -1, v82
	s_lshr_b32 s0, s37, 2
	s_and_b32 s1, s37, 3
	v_and_b32_e32 v126, 31, v82
	v_lshrrev_b32_e32 v127, 5, v82
	s_lshl_b32 s24, s0, 7
	s_add_i32 s24, s24, 0x15300
	v_lshl_add_u32 v126, v126, 2, s24
	ds_read_b32 v83, v126
	s_lshl_b32 s24, s1, 7
	s_add_i32 s24, s24, 0x14c00
	v_lshl_add_u32 v65, v127, 4, s24
	ds_read_b128 v[88:91], v65
	ds_read_b128 v[92:95], v65 offset:32
	ds_read_b128 v[96:99], v65 offset:64
	ds_read_b128 v[100:103], v65 offset:96
	v_mov_b32_e32 v63, 0x15000
	v_lshl_add_u32 v63, v127, 5, v63
	s_mul_i32 s24, s1, 0x1400
	v_lshl_add_u32 v64, v82, 4, s24
	ds_read_b128 v[84:87], v63
	ds_read_b64 v[104:105], v63 offset:256
	ds_read_b64 v[114:115], v63 offset:264
	s_waitcnt lgkmcnt(0)
	v_fma_f32 v84, v83, v84, v104
	v_fma_f32 v85, v83, v85, v105
	v_fma_f32 v86, v83, v86, v114
	v_fma_f32 v87, v83, v87, v115
	v_max_f32_e32 v84, 0, v84
	v_max_f32_e32 v85, 0, v85
	v_max_f32_e32 v86, 0, v86
	v_max_f32_e32 v87, 0, v87
	v_cvt_pk_f16_f32 v122, v84, v85
	v_cvt_pk_f16_f32 v123, v86, v87
	ds_read_b128 v[84:87], v63 offset:16
	ds_read_b64 v[104:105], v63 offset:272
	ds_read_b64 v[114:115], v63 offset:280
	ds_read_b128 v[118:121], v64
	s_waitcnt lgkmcnt(0)
	v_fma_f32 v84, v83, v84, v104
	v_fma_f32 v85, v83, v85, v105
	v_fma_f32 v86, v83, v86, v114
	v_fma_f32 v87, v83, v87, v115
	v_max_f32_e32 v84, 0, v84
	v_max_f32_e32 v85, 0, v85
	v_max_f32_e32 v86, 0, v86
	v_max_f32_e32 v87, 0, v87
	v_cvt_pk_f16_f32 v124, v84, v85
	v_cvt_pk_f16_f32 v125, v86, v87
	s_nop 1
	v_mfma_f32_32x32x16_f16 v[88:103], v[118:121], v[122:125], v[88:103]
	ds_read_b128 v[84:87], v63 offset:64
	ds_read_b64 v[104:105], v63 offset:320
	ds_read_b64 v[114:115], v63 offset:328
	s_waitcnt lgkmcnt(0)
	v_fma_f32 v84, v83, v84, v104
	v_fma_f32 v85, v83, v85, v105
	v_fma_f32 v86, v83, v86, v114
	v_fma_f32 v87, v83, v87, v115
	v_max_f32_e32 v84, 0, v84
	v_max_f32_e32 v85, 0, v85
	v_max_f32_e32 v86, 0, v86
	v_max_f32_e32 v87, 0, v87
	v_cvt_pk_f16_f32 v122, v84, v85
	v_cvt_pk_f16_f32 v123, v86, v87
	ds_read_b128 v[84:87], v63 offset:80
	ds_read_b64 v[104:105], v63 offset:336
	ds_read_b64 v[114:115], v63 offset:344
	ds_read_b128 v[118:121], v64 offset:1024
	s_waitcnt lgkmcnt(0)
	v_fma_f32 v84, v83, v84, v104
	v_fma_f32 v85, v83, v85, v105
	v_fma_f32 v86, v83, v86, v114
	v_fma_f32 v87, v83, v87, v115
	v_max_f32_e32 v84, 0, v84
	v_max_f32_e32 v85, 0, v85
	v_max_f32_e32 v86, 0, v86
	v_max_f32_e32 v87, 0, v87
	v_cvt_pk_f16_f32 v124, v84, v85
	v_cvt_pk_f16_f32 v125, v86, v87
	s_nop 1
	v_mfma_f32_32x32x16_f16 v[88:103], v[118:121], v[122:125], v[88:103]
	ds_read_b128 v[84:87], v63 offset:128
	ds_read_b64 v[104:105], v63 offset:384
	ds_read_b64 v[114:115], v63 offset:392
	s_waitcnt lgkmcnt(0)
	v_fma_f32 v84, v83, v84, v104
	v_fma_f32 v85, v83, v85, v105
	v_fma_f32 v86, v83, v86, v114
	v_fma_f32 v87, v83, v87, v115
	v_max_f32_e32 v84, 0, v84
	v_max_f32_e32 v85, 0, v85
	v_max_f32_e32 v86, 0, v86
	v_max_f32_e32 v87, 0, v87
	v_cvt_pk_f16_f32 v122, v84, v85
	v_cvt_pk_f16_f32 v123, v86, v87
	ds_read_b128 v[84:87], v63 offset:144
	ds_read_b64 v[104:105], v63 offset:400
	ds_read_b64 v[114:115], v63 offset:408
	ds_read_b128 v[118:121], v64 offset:2048
	s_waitcnt lgkmcnt(0)
	v_fma_f32 v84, v83, v84, v104
	v_fma_f32 v85, v83, v85, v105
	v_fma_f32 v86, v83, v86, v114
	v_fma_f32 v87, v83, v87, v115
	v_max_f32_e32 v84, 0, v84
	v_max_f32_e32 v85, 0, v85
	v_max_f32_e32 v86, 0, v86
	v_max_f32_e32 v87, 0, v87
	v_cvt_pk_f16_f32 v124, v84, v85
	v_cvt_pk_f16_f32 v125, v86, v87
	s_nop 1
	v_mfma_f32_32x32x16_f16 v[88:103], v[118:121], v[122:125], v[88:103]
	ds_read_b128 v[84:87], v63 offset:192
	ds_read_b64 v[104:105], v63 offset:448
	ds_read_b64 v[114:115], v63 offset:456
	s_waitcnt lgkmcnt(0)
	v_fma_f32 v84, v83, v84, v104
	v_fma_f32 v85, v83, v85, v105
	v_fma_f32 v86, v83, v86, v114
	v_fma_f32 v87, v83, v87, v115
	v_max_f32_e32 v84, 0, v84
	v_max_f32_e32 v85, 0, v85
	v_max_f32_e32 v86, 0, v86
	v_max_f32_e32 v87, 0, v87
	v_cvt_pk_f16_f32 v122, v84, v85
	v_cvt_pk_f16_f32 v123, v86, v87
	ds_read_b128 v[84:87], v63 offset:208
	ds_read_b64 v[104:105], v63 offset:464
	ds_read_b64 v[114:115], v63 offset:472
	ds_read_b128 v[118:121], v64 offset:3072
	s_waitcnt lgkmcnt(0)
	v_fma_f32 v84, v83, v84, v104
	v_fma_f32 v85, v83, v85, v105
	v_fma_f32 v86, v83, v86, v114
	v_fma_f32 v87, v83, v87, v115
	v_max_f32_e32 v84, 0, v84
	v_max_f32_e32 v85, 0, v85
	v_max_f32_e32 v86, 0, v86
	v_max_f32_e32 v87, 0, v87
	v_cvt_pk_f16_f32 v124, v84, v85
	v_cvt_pk_f16_f32 v125, v86, v87
	s_nop 1
	v_mfma_f32_32x32x16_f16 v[88:103], v[118:121], v[122:125], v[88:103]
	s_lshl_b32 s24, s37, 12
	s_add_i32 s24, s24, 0x15440
	v_lshl_add_u32 v65, v82, 4, s24
	s_nop 7
	s_nop 4
	ds_write_b128 v65, v[88:91]
	ds_write_b128 v65, v[92:95] offset:1024
	ds_write_b128 v65, v[96:99] offset:2048
	ds_write_b128 v65, v[100:103] offset:3072
.Lh1_done:
	s_branch .LBB0_74

.LBB0_120:
	s_cmpk_gt_u32 s33, 0x7f
	s_waitcnt lgkmcnt(0)
	s_cbranch_scc1 .Lmlp_others
	v_mbcnt_lo_u32_b32 v92, -1, 0
	v_mbcnt_hi_u32_b32 v92, -1, v92
	s_lshl_b32 s0, s31, 9
	s_add_i32 s0, s0, 0x15440
	v_lshl_add_u32 v95, v92, 4, s0
	v_ashrrev_i32_e32 v0, 5, v92
	s_waitcnt vmcnt(0)
	v_and_or_b32 v37, v92, 31, s31
	v_lshlrev_b32_e32 v38, 4, v0
	v_add_u32_e32 v93, 0x14c00, v38
	v_lshlrev_b32_e32 v94, 4, v92
	v_lshlrev_b32_e32 v24, 5, v37
	s_mov_b32 s0, 0x13400
	v_add3_u32 v28, v24, v38, s0
	ds_read_b128 v[80:83], v93 offset:992
	ds_read_b128 v[20:23], v94 offset:4096
	s_waitcnt lgkmcnt(0)
	s_barrier
	ds_read_b128 v[88:91], v28
	ds_read_b128 v[0:3], v95
	ds_read_b128 v[4:7], v95 offset:1024
	ds_read_b128 v[8:11], v95 offset:2048
	ds_read_b128 v[12:15], v95 offset:3072
	ds_read_b128 v[16:19], v95 offset:4096
	v_cmp_gt_u32_e32 vcc, 32, v92
	s_waitcnt lgkmcnt(0)
	v_mfma_f32_32x32x16_f16 v[0:15], v[20:23], v[88:91], v[0:15]
	ds_read_b128 v[20:23], v95 offset:5120
	ds_read_b128 v[24:27], v95 offset:6144
	ds_read_b128 v[28:31], v95 offset:7168
	ds_read_b128 v[64:67], v95 offset:8192
	s_waitcnt lgkmcnt(1)
	s_nop 0
	s_nop 0
	s_nop 0
	s_nop 3
	v_max_f32_e32 v4, v4, v4
	v_max_f32_e32 v5, v5, v5
	v_max_f32_e32 v6, v6, v6
	v_max_f32_e32 v7, v7, v7
	v_max_f32_e32 v4, 0, v4
	v_max_f32_e32 v5, 0, v5
	s_waitcnt lgkmcnt(0)
	s_nop 0
	v_max_f32_e32 v6, 0, v6
	v_max_f32_e32 v7, 0, v7
	v_max_f32_e32 v2, v2, v2
	v_max_f32_e32 v3, v3, v3
	v_max_f32_e32 v2, 0, v2
	v_max_f32_e32 v3, 0, v3
	v_max_f32_e32 v0, v0, v0
	s_waitcnt lgkmcnt(0)
	s_nop 0
	s_nop 0
	ds_read_b128 v[48:51], v94 offset:9216
	v_max_f32_e32 v1, v1, v1
	v_max_f32_e32 v0, 0, v0
	v_max_f32_e32 v1, 0, v1
	s_waitcnt lgkmcnt(1)
	s_nop 0
	s_nop 0
	s_waitcnt lgkmcnt(0)
	v_mfma_f32_32x32x16_f16 v[16:31], v[48:51], v[88:91], v[16:31]
	ds_read_b128 v[68:71], v95 offset:9216
	ds_read_b128 v[72:75], v95 offset:10240
	ds_read_b128 v[76:79], v95 offset:11264
	ds_read_b128 v[48:51], v95 offset:12288
	s_nop 0
	s_waitcnt lgkmcnt(1)
	s_nop 0
	s_waitcnt lgkmcnt(0)
	s_nop 0
	s_nop 0
	s_nop 0
	s_waitcnt lgkmcnt(0)
	s_nop 0
	ds_read_b128 v[32:35], v94 offset:14336
	s_nop 0
	s_waitcnt lgkmcnt(1)
	s_nop 0
	s_waitcnt lgkmcnt(0)
	v_mfma_f32_32x32x16_f16 v[64:79], v[32:35], v[88:91], v[64:79]
	ds_read_b128 v[52:55], v95 offset:13312
	ds_read_b128 v[56:59], v95 offset:14336
	ds_read_b128 v[60:63], v95 offset:15360
	ds_read_b128 v[32:35], v93 offset:512
	s_waitcnt lgkmcnt(1)
	s_nop 0
	s_nop 0
	s_nop 0
	s_waitcnt lgkmcnt(0)
	s_nop 0
	s_nop 0
	ds_read_b128 v[44:47], v94 offset:19456
	s_waitcnt lgkmcnt(1)
	s_nop 0
	v_cvt_pk_f16_f32 v87, v6, v7
	v_cvt_pk_f16_f32 v86, v4, v5
	v_max_f32_e32 v4, v12, v12
	v_max_f32_e32 v5, v13, v13
	v_max_f32_e32 v6, v14, v14
	v_max_f32_e32 v7, v15, v15
	v_max_f32_e32 v4, 0, v4
	s_waitcnt lgkmcnt(1)
	s_nop 0
	v_max_f32_e32 v5, 0, v5
	v_max_f32_e32 v6, 0, v6
	v_max_f32_e32 v7, 0, v7
	v_cvt_pk_f16_f32 v85, v2, v3
	v_max_f32_e32 v2, v10, v10
	v_max_f32_e32 v3, v11, v11
	v_max_f32_e32 v2, 0, v2
	s_waitcnt lgkmcnt(0)
	v_mfma_f32_32x32x16_f16 v[48:63], v[44:47], v[88:91], v[48:63]
	v_cvt_pk_f16_f32 v91, v6, v7
	v_cvt_pk_f16_f32 v90, v4, v5
	v_max_f32_e32 v4, v20, v20
	v_max_f32_e32 v5, v21, v21
	v_max_f32_e32 v6, v22, v22
	v_max_f32_e32 v7, v23, v23
	v_max_f32_e32 v3, 0, v3
	v_max_f32_e32 v4, 0, v4
	v_max_f32_e32 v5, 0, v5
	v_max_f32_e32 v6, 0, v6
	v_max_f32_e32 v7, 0, v7
	v_cvt_pk_f16_f32 v89, v2, v3
	v_max_f32_e32 v2, v18, v18
	v_max_f32_e32 v3, v19, v19
	v_cvt_pk_f16_f32 v19, v6, v7
	v_cvt_pk_f16_f32 v18, v4, v5
	v_max_f32_e32 v4, v28, v28
	v_max_f32_e32 v5, v29, v29
	v_max_f32_e32 v6, v30, v30
	v_max_f32_e32 v7, v31, v31
	v_max_f32_e32 v4, 0, v4
	v_max_f32_e32 v5, 0, v5
	v_max_f32_e32 v6, 0, v6
	v_max_f32_e32 v7, 0, v7
	v_cvt_pk_f16_f32 v84, v0, v1
	v_max_f32_e32 v0, v8, v8
	v_max_f32_e32 v1, v9, v9
	v_cvt_pk_f16_f32 v23, v6, v7
	v_cvt_pk_f16_f32 v22, v4, v5
	v_max_f32_e32 v4, v68, v68
	v_max_f32_e32 v5, v69, v69
	v_max_f32_e32 v6, v70, v70
	v_max_f32_e32 v7, v71, v71
	v_max_f32_e32 v0, 0, v0
	v_max_f32_e32 v1, 0, v1
	v_max_f32_e32 v2, 0, v2
	v_max_f32_e32 v3, 0, v3
	v_max_f32_e32 v4, 0, v4
	v_max_f32_e32 v5, 0, v5
	v_max_f32_e32 v6, 0, v6
	v_max_f32_e32 v7, 0, v7
	v_cvt_pk_f16_f32 v88, v0, v1
	v_max_f32_e32 v0, v16, v16
	v_max_f32_e32 v1, v17, v17
	v_cvt_pk_f16_f32 v17, v2, v3
	v_max_f32_e32 v2, v26, v26
	v_max_f32_e32 v3, v27, v27
	v_cvt_pk_f16_f32 v27, v6, v7
	v_cvt_pk_f16_f32 v26, v4, v5
	ds_read_b128 v[4:7], v94 offset:20480
	v_max_f32_e32 v0, 0, v0
	v_max_f32_e32 v1, 0, v1
	v_cvt_pk_f16_f32 v16, v0, v1
	v_max_f32_e32 v0, v24, v24
	v_max_f32_e32 v1, v25, v25
	v_max_f32_e32 v0, 0, v0
	v_max_f32_e32 v1, 0, v1
	v_cvt_pk_f16_f32 v20, v0, v1
	v_max_f32_e32 v0, v64, v64
	v_max_f32_e32 v1, v65, v65
	ds_read_b128 v[36:39], v93 offset:544
	ds_read_b128 v[40:43], v93 offset:576
	ds_read_b128 v[44:47], v93 offset:608
	v_max_f32_e32 v0, 0, v0
	v_max_f32_e32 v1, 0, v1
	v_cvt_pk_f16_f32 v24, v0, v1
	v_max_f32_e32 v0, v72, v72
	v_max_f32_e32 v2, 0, v2
	v_max_f32_e32 v3, 0, v3
	v_max_f32_e32 v12, 0, v0
	v_max_f32_e32 v0, v73, v73
	v_cvt_pk_f16_f32 v21, v2, v3
	v_max_f32_e32 v2, v66, v66
	v_max_f32_e32 v3, v67, v67
	v_max_f32_e32 v13, 0, v0
	v_max_f32_e32 v0, v74, v74
	v_max_f32_e32 v2, 0, v2
	v_max_f32_e32 v3, 0, v3
	v_max_f32_e32 v14, 0, v0
	v_max_f32_e32 v0, v75, v75
	s_waitcnt lgkmcnt(0)
	v_mfma_f32_32x32x16_f16 v[32:47], v[4:7], v[84:87], v[32:47]
	v_cvt_pk_f16_f32 v25, v2, v3
	v_max_f32_e32 v15, 0, v0
	v_max_f32_e32 v0, v76, v76
	v_max_f32_e32 v1, v77, v77
	v_max_f32_e32 v2, v78, v78
	v_max_f32_e32 v3, v79, v79
	v_max_f32_e32 v0, 0, v0
	v_max_f32_e32 v1, 0, v1
	v_max_f32_e32 v2, 0, v2
	v_max_f32_e32 v3, 0, v3
	v_cvt_pk_f16_f32 v31, v2, v3
	v_cvt_pk_f16_f32 v30, v0, v1
	ds_read_b128 v[0:3], v93 offset:640
	ds_read_b128 v[8:11], v94 offset:21504
	v_max_f32_e32 v4, v48, v48
	v_cvt_pk_f16_f32 v28, v12, v13
	v_max_f32_e32 v12, 0, v4
	v_max_f32_e32 v4, v49, v49
	v_max_f32_e32 v13, 0, v4
	ds_read_b128 v[4:7], v94 offset:22528
	s_waitcnt lgkmcnt(1)
	v_mfma_f32_32x32x16_f16 v[32:47], v[8:11], v[88:91], v[32:47]
	v_max_f32_e32 v8, v50, v50
	v_cvt_pk_f16_f32 v29, v14, v15
	v_max_f32_e32 v14, 0, v8
	v_max_f32_e32 v8, v51, v51
	v_max_f32_e32 v15, 0, v8
	v_max_f32_e32 v8, v52, v52
	v_max_f32_e32 v48, 0, v8
	ds_read_b128 v[8:11], v94 offset:23552
	s_waitcnt lgkmcnt(1)
	v_mfma_f32_32x32x16_f16 v[32:47], v[4:7], v[16:19], v[32:47]
	v_max_f32_e32 v4, v53, v53
	v_max_f32_e32 v49, 0, v4
	v_max_f32_e32 v4, v54, v54
	v_max_f32_e32 v50, 0, v4
	v_max_f32_e32 v4, v55, v55
	v_max_f32_e32 v51, 0, v4
	ds_read_b128 v[4:7], v94 offset:24576
	s_waitcnt lgkmcnt(1)
	v_mfma_f32_32x32x16_f16 v[32:47], v[8:11], v[20:23], v[32:47]
	v_max_f32_e32 v8, v56, v56
	v_cvt_pk_f16_f32 v51, v50, v51
	v_cvt_pk_f16_f32 v50, v48, v49
	v_cvt_pk_f16_f32 v48, v12, v13
	v_max_f32_e32 v12, 0, v8
	ds_read_b128 v[8:11], v94 offset:25600
	v_cvt_pk_f16_f32 v49, v14, v15
	s_waitcnt lgkmcnt(1)
	v_mfma_f32_32x32x16_f16 v[32:47], v[4:7], v[24:27], v[32:47]
	v_max_f32_e32 v4, v57, v57
	v_max_f32_e32 v13, 0, v4
	v_max_f32_e32 v4, v58, v58
	v_max_f32_e32 v14, 0, v4
	v_max_f32_e32 v4, v59, v59
	v_max_f32_e32 v15, 0, v4
	ds_read_b128 v[4:7], v94 offset:26624
	s_waitcnt lgkmcnt(1)
	v_mfma_f32_32x32x16_f16 v[32:47], v[8:11], v[28:31], v[32:47]
	v_max_f32_e32 v8, v60, v60
	v_max_f32_e32 v52, 0, v8
	v_max_f32_e32 v8, v61, v61
	v_max_f32_e32 v53, 0, v8
	v_max_f32_e32 v8, v62, v62
	v_max_f32_e32 v54, 0, v8
	ds_read_b128 v[8:11], v94 offset:27648
	s_waitcnt lgkmcnt(1)
	v_mfma_f32_32x32x16_f16 v[32:47], v[4:7], v[48:51], v[32:47]
	ds_read_b128 v[56:59], v94 offset:28672
	v_max_f32_e32 v4, v63, v63
	v_max_f32_e32 v4, 0, v4
	v_cvt_pk_f16_f32 v55, v54, v4
	v_cvt_pk_f16_f32 v54, v52, v53
	v_cvt_pk_f16_f32 v53, v14, v15
	v_cvt_pk_f16_f32 v52, v12, v13
	s_waitcnt lgkmcnt(1)
	s_nop 0
	v_mfma_f32_32x32x16_f16 v[32:47], v[8:11], v[52:55], v[32:47]
	ds_read_b128 v[4:7], v93 offset:672
	ds_read_b128 v[8:11], v93 offset:704
	ds_read_b128 v[12:15], v93 offset:736
	ds_read_b128 v[60:63], v94 offset:29696
	ds_read_b128 v[64:67], v93 offset:768
	s_waitcnt lgkmcnt(2)
	v_mfma_f32_32x32x16_f16 v[0:15], v[56:59], v[84:87], v[0:15]
	s_waitcnt lgkmcnt(1)
	v_mfma_f32_32x32x16_f16 v[0:15], v[60:63], v[88:91], v[0:15]
	ds_read_b128 v[56:59], v94 offset:30720
	ds_read_b128 v[60:63], v94 offset:31744
	s_waitcnt lgkmcnt(1)
	v_mfma_f32_32x32x16_f16 v[0:15], v[56:59], v[16:19], v[0:15]
	s_waitcnt lgkmcnt(0)
	v_mfma_f32_32x32x16_f16 v[0:15], v[60:63], v[20:23], v[0:15]
	ds_read_b128 v[16:19], v94 offset:32768
	ds_read_b128 v[20:23], v94 offset:33792
	s_waitcnt lgkmcnt(1)
	v_mfma_f32_32x32x16_f16 v[0:15], v[16:19], v[24:27], v[0:15]
	s_waitcnt lgkmcnt(0)
	v_mfma_f32_32x32x16_f16 v[0:15], v[20:23], v[28:31], v[0:15]
	ds_read_b128 v[16:19], v94 offset:34816
	ds_read_b128 v[20:23], v94 offset:35840
	s_waitcnt lgkmcnt(1)
	v_mfma_f32_32x32x16_f16 v[0:15], v[16:19], v[48:51], v[0:15]
	v_max_f32_e32 v16, v32, v32
	v_max_f32_e32 v16, 0, v16
	v_max_f32_e32 v17, v33, v33
	v_fma_f32 v16, v64, v16, 0
	v_max_f32_e32 v17, 0, v17
	v_fmac_f32_e32 v16, v65, v17
	v_max_f32_e32 v17, v34, v34
	s_waitcnt lgkmcnt(0)
	v_mfma_f32_32x32x16_f16 v[0:15], v[20:23], v[52:55], v[0:15]
	v_max_f32_e32 v17, 0, v17
	ds_read_b128 v[18:21], v93 offset:800
	ds_read_b128 v[22:25], v93 offset:832
	v_fmac_f32_e32 v16, v66, v17
	v_max_f32_e32 v17, v35, v35
	v_max_f32_e32 v17, 0, v17
	v_fmac_f32_e32 v16, v67, v17
	v_max_f32_e32 v17, v36, v36
	v_max_f32_e32 v17, 0, v17
	s_waitcnt lgkmcnt(1)
	v_fmac_f32_e32 v16, v18, v17
	v_max_f32_e32 v17, v37, v37
	v_max_f32_e32 v17, 0, v17
	v_fmac_f32_e32 v16, v19, v17
	v_max_f32_e32 v17, v38, v38
	v_max_f32_e32 v17, 0, v17
	v_fmac_f32_e32 v16, v20, v17
	v_max_f32_e32 v17, v39, v39
	v_max_f32_e32 v17, 0, v17
	v_fmac_f32_e32 v16, v21, v17
	v_max_f32_e32 v17, v40, v40
	v_max_f32_e32 v17, 0, v17
	s_waitcnt lgkmcnt(0)
	v_fmac_f32_e32 v16, v22, v17
	v_max_f32_e32 v17, v41, v41
	v_max_f32_e32 v17, 0, v17
	v_fmac_f32_e32 v16, v23, v17
	v_max_f32_e32 v17, v42, v42
	v_max_f32_e32 v17, 0, v17
	ds_read_b128 v[18:21], v93 offset:864
	v_fmac_f32_e32 v16, v24, v17
	v_max_f32_e32 v17, v43, v43
	v_max_f32_e32 v17, 0, v17
	v_fmac_f32_e32 v16, v25, v17
	v_max_f32_e32 v17, v44, v44
	v_max_f32_e32 v17, 0, v17
	ds_read_b128 v[22:25], v93 offset:896
	s_waitcnt lgkmcnt(1)
	v_fmac_f32_e32 v16, v18, v17
	v_max_f32_e32 v17, v45, v45
	v_max_f32_e32 v17, 0, v17
	v_fmac_f32_e32 v16, v19, v17
	v_max_f32_e32 v17, v46, v46
	v_max_f32_e32 v17, 0, v17
	v_fmac_f32_e32 v16, v20, v17
	v_max_f32_e32 v17, v47, v47
	v_max_f32_e32 v17, 0, v17
	v_max_f32_e32 v0, v0, v0
	v_fmac_f32_e32 v16, v21, v17
	v_max_f32_e32 v0, 0, v0
	s_waitcnt lgkmcnt(0)
	v_fmac_f32_e32 v16, v22, v0
	v_max_f32_e32 v0, v1, v1
	v_max_f32_e32 v0, 0, v0
	v_fmac_f32_e32 v16, v23, v0
	v_max_f32_e32 v0, v2, v2
	v_max_f32_e32 v0, 0, v0
	v_fmac_f32_e32 v16, v24, v0
	v_max_f32_e32 v0, v3, v3
	v_max_f32_e32 v17, 0, v0
	ds_read_b128 v[0:3], v93 offset:928
	ds_read_b128 v[18:21], v93 offset:960
	v_max_f32_e32 v4, v4, v4
	v_fmac_f32_e32 v16, v25, v17
	v_max_f32_e32 v4, 0, v4
	s_waitcnt lgkmcnt(1)
	v_fmac_f32_e32 v16, v0, v4
	v_max_f32_e32 v0, v5, v5
	v_max_f32_e32 v0, 0, v0
	v_fmac_f32_e32 v16, v1, v0
	v_max_f32_e32 v0, v6, v6
	v_max_f32_e32 v0, 0, v0
	v_fmac_f32_e32 v16, v2, v0
	v_max_f32_e32 v0, v7, v7
	v_max_f32_e32 v0, 0, v0
	v_fmac_f32_e32 v16, v3, v0
	v_max_f32_e32 v0, v8, v8
	v_max_f32_e32 v0, 0, v0
	s_waitcnt lgkmcnt(0)
	v_fmac_f32_e32 v16, v18, v0
	v_max_f32_e32 v0, v9, v9
	v_max_f32_e32 v0, 0, v0
	v_fmac_f32_e32 v16, v19, v0
	v_max_f32_e32 v0, v10, v10
	v_max_f32_e32 v0, 0, v0
	v_fmac_f32_e32 v16, v20, v0
	v_max_f32_e32 v0, v11, v11
	v_max_f32_e32 v0, 0, v0
	v_fmac_f32_e32 v16, v21, v0
	v_max_f32_e32 v0, v12, v12
	v_max_f32_e32 v0, 0, v0
	v_fmac_f32_e32 v16, v80, v0
	v_max_f32_e32 v0, v13, v13
	v_max_f32_e32 v0, 0, v0
	v_fmac_f32_e32 v16, v81, v0
	v_max_f32_e32 v0, v14, v14
	v_max_f32_e32 v0, 0, v0
	v_fmac_f32_e32 v16, v82, v0
	v_max_f32_e32 v0, v15, v15
	v_max_f32_e32 v0, 0, v0
	v_fmac_f32_e32 v16, v83, v0
	v_mov_b32_e32 v0, v16
	s_nop 1
	v_permlane32_swap_b32_e32 v16, v0
	s_and_saveexec_b64 s[0:1], vcc
	s_cbranch_execz .LBB0_123
	s_mov_b32 s0, s88
	v_add_f32_e32 v0, v16, v0
	s_waitcnt lgkmcnt(0)
	v_add_f32_e32 v0, s0, v0
	v_mul_f32_e32 v0, 0xbfb8aa3b, v0
	v_exp_f32_e32 v1, v0
	s_or_b32 s0, s31, s30
	v_or_b32_e32 v0, s0, v92
	v_add_f32_e32 v2, 1.0, v1
	v_div_scale_f32 v3, s[0:1], v2, v2, 1.0
	v_rcp_f32_e32 v4, v3
	v_div_scale_f32 v5, vcc, 1.0, v2, 1.0
	v_ashrrev_i32_e32 v1, 31, v0
	v_fma_f32 v6, -v3, v4, 1.0
	v_fmac_f32_e32 v4, v6, v4
	v_mul_f32_e32 v6, v5, v4
	v_fma_f32 v7, -v3, v6, v5
	v_fmac_f32_e32 v6, v7, v4
	v_fma_f32 v3, -v3, v6, v5
	v_div_fmas_f32 v3, v3, v4, v6
	v_div_fixup_f32 v2, v3, v2, 1.0
	v_lshl_add_u64 v[0:1], v[0:1], 2, s[22:23]
	global_store_dword v[0:1], v2, off

	.amdhsa_kernel _Z6k_dlrmPKiS0_S0_S0_S0_S0_S0_PKfS2_S2_S2_S2_S2_S2_S2_S2_S2_S2_S2_S2_S2_S2_S2_Pf
		.amdhsa_group_segment_fixed_size 119872
		.amdhsa_private_segment_fixed_size 0
		.amdhsa_kernarg_size 192
		.amdhsa_user_sgpr_count 2
		.amdhsa_user_sgpr_dispatch_ptr 0
		.amdhsa_user_sgpr_queue_ptr 0
		.amdhsa_user_sgpr_kernarg_segment_ptr 1
		.amdhsa_user_sgpr_dispatch_id 0
		.amdhsa_user_sgpr_kernarg_preload_length 0
		.amdhsa_user_sgpr_kernarg_preload_offset 0
		.amdhsa_user_sgpr_private_segment_size 0
		.amdhsa_uses_dynamic_stack 0
		.amdhsa_enable_private_segment 0
		.amdhsa_system_sgpr_workgroup_id_x 1
		.amdhsa_system_sgpr_workgroup_id_y 0
		.amdhsa_system_sgpr_workgroup_id_z 0
		.amdhsa_system_sgpr_workgroup_info 0
		.amdhsa_system_vgpr_workitem_id 0
		.amdhsa_next_free_vgpr 128
		.amdhsa_next_free_sgpr 96
		.amdhsa_accum_offset 128
		.amdhsa_reserve_vcc 1
		.amdhsa_float_round_mode_32 0
		.amdhsa_float_round_mode_16_64 0
		.amdhsa_float_denorm_mode_32 3
		.amdhsa_float_denorm_mode_16_64 3
		.amdhsa_dx10_clamp 1
		.amdhsa_ieee_mode 1
		.amdhsa_fp16_overflow 0
		.amdhsa_tg_split 0
		.amdhsa_exception_fp_ieee_invalid_op 0
		.amdhsa_exception_fp_denorm_src 0
		.amdhsa_exception_fp_ieee_div_zero 0
		.amdhsa_exception_fp_ieee_overflow 0
		.amdhsa_exception_fp_ieee_underflow 0
		.amdhsa_exception_fp_ieee_inexact 0
		.amdhsa_exception_int_div_zero 0
	.end_amdhsa_kernel

amdhsa.kernels:
  - .agpr_count:     0
    .args:
      - .actual_access:  read_only
        .address_space:  global
        .offset:         0
        .size:           8
        .value_kind:     global_buffer
      - .actual_access:  read_only
        .address_space:  global
        .offset:         8
        .size:           8
        .value_kind:     global_buffer
      - .actual_access:  read_only
        .address_space:  global
        .offset:         16
        .size:           8
        .value_kind:     global_buffer
      - .actual_access:  read_only
        .address_space:  global
        .offset:         24
        .size:           8
        .value_kind:     global_buffer
      - .actual_access:  read_only
        .address_space:  global
        .offset:         32
        .size:           8
        .value_kind:     global_buffer
      - .actual_access:  read_only
        .address_space:  global
        .offset:         40
        .size:           8
        .value_kind:     global_buffer
      - .actual_access:  read_only
        .address_space:  global
        .offset:         48
        .size:           8
        .value_kind:     global_buffer
      - .actual_access:  read_only
        .address_space:  global
        .offset:         56
        .size:           8
        .value_kind:     global_buffer
      - .actual_access:  read_only
        .address_space:  global
        .offset:         64
        .size:           8
        .value_kind:     global_buffer
      - .actual_access:  read_only
        .address_space:  global
        .offset:         72
        .size:           8
        .value_kind:     global_buffer
      - .actual_access:  read_only
        .address_space:  global
        .offset:         80
        .size:           8
        .value_kind:     global_buffer
      - .actual_access:  read_only
        .address_space:  global
        .offset:         88
        .size:           8
        .value_kind:     global_buffer
      - .actual_access:  read_only
        .address_space:  global
        .offset:         96
        .size:           8
        .value_kind:     global_buffer
      - .actual_access:  read_only
        .address_space:  global
        .offset:         104
        .size:           8
        .value_kind:     global_buffer
      - .actual_access:  read_only
        .address_space:  global
        .offset:         112
        .size:           8
        .value_kind:     global_buffer
      - .actual_access:  read_only
        .address_space:  global
        .offset:         120
        .size:           8
        .value_kind:     global_buffer
      - .actual_access:  read_only
        .address_space:  global
        .offset:         128
        .size:           8
        .value_kind:     global_buffer
      - .actual_access:  read_only
        .address_space:  global
        .offset:         136
        .size:           8
        .value_kind:     global_buffer
      - .actual_access:  read_only
        .address_space:  global
        .offset:         144
        .size:           8
        .value_kind:     global_buffer
      - .actual_access:  read_only
        .address_space:  global
        .offset:         152
        .size:           8
        .value_kind:     global_buffer
      - .actual_access:  read_only
        .address_space:  global
        .offset:         160
        .size:           8
        .value_kind:     global_buffer
      - .actual_access:  read_only
        .address_space:  global
        .offset:         168
        .size:           8
        .value_kind:     global_buffer
      - .actual_access:  read_only
        .address_space:  global
        .offset:         176
        .size:           8
        .value_kind:     global_buffer
      - .actual_access:  write_only
        .address_space:  global
        .offset:         184
        .size:           8
        .value_kind:     global_buffer
    .group_segment_fixed_size: 119872
    .kernarg_segment_align: 8
    .kernarg_segment_size: 192
    .language:       OpenCL C
    .language_version:
      - 2
      - 0
    .max_flat_workgroup_size: 1024
    .name:           _Z6k_dlrmPKiS0_S0_S0_S0_S0_S0_PKfS2_S2_S2_S2_S2_S2_S2_S2_S2_S2_S2_S2_S2_S2_S2_Pf
    .private_segment_fixed_size: 0
    .sgpr_count:     44
    .sgpr_spill_count: 0
    .symbol:         _Z6k_dlrmPKiS0_S0_S0_S0_S0_S0_PKfS2_S2_S2_S2_S2_S2_S2_S2_S2_S2_S2_S2_S2_S2_S2_Pf.kd
    .uniform_work_group_size: 1
    .uses_dynamic_stack: false
    .vgpr_count:     128
    .vgpr_spill_count: 0
    .wavefront_size: 64
